# sgpr32
# baseline (speedup 1.0000x reference)
	.amdhsa_kernel _Z10gae_kernelPKfPKiS2_S0_S0_S0_PfS3_
		.amdhsa_group_segment_fixed_size 54016
		.amdhsa_private_segment_fixed_size 0
		.amdhsa_kernarg_size 64
		.amdhsa_user_sgpr_count 2
		.amdhsa_user_sgpr_dispatch_ptr 0
		.amdhsa_user_sgpr_queue_ptr 0
		.amdhsa_user_sgpr_kernarg_segment_ptr 1
		.amdhsa_user_sgpr_dispatch_id 0
		.amdhsa_user_sgpr_kernarg_preload_length 0
		.amdhsa_user_sgpr_kernarg_preload_offset 0
		.amdhsa_user_sgpr_private_segment_size 0
		.amdhsa_uses_dynamic_stack 0
		.amdhsa_enable_private_segment 0
		.amdhsa_system_sgpr_workgroup_id_x 1
		.amdhsa_system_sgpr_workgroup_id_y 0
		.amdhsa_system_sgpr_workgroup_id_z 0
		.amdhsa_system_sgpr_workgroup_info 0
		.amdhsa_system_vgpr_workitem_id 0
		.amdhsa_next_free_vgpr 80
		.amdhsa_next_free_sgpr 32
		.amdhsa_accum_offset 76
		.amdhsa_reserve_vcc 1
		.amdhsa_float_round_mode_32 0
		.amdhsa_float_round_mode_16_64 0
		.amdhsa_float_denorm_mode_32 3
		.amdhsa_float_denorm_mode_16_64 3
		.amdhsa_dx10_clamp 1
		.amdhsa_ieee_mode 1
		.amdhsa_fp16_overflow 0
		.amdhsa_tg_split 0
		.amdhsa_exception_fp_ieee_invalid_op 0
		.amdhsa_exception_fp_denorm_src 0
		.amdhsa_exception_fp_ieee_div_zero 0
		.amdhsa_exception_fp_ieee_overflow 0
		.amdhsa_exception_fp_ieee_underflow 0
		.amdhsa_exception_fp_ieee_inexact 0
		.amdhsa_exception_int_div_zero 0
	.end_amdhsa_kernel
